# E13: E12 + first vmcnt wait of each unit's peeled K-iteration relaxed to 8+lower bound of epilogue VMEM ops (no epilogue-store drain at unit start); P1 pre-loop vmcnt(0) dropped
# speedup vs baseline: 1.0170x; 1.0031x over previous
.LBB0_161:
	s_cmp_eq_u32 s56, 0
	s_cselect_b32 s22, s55, s54
	s_cselect_b32 s25, s36, s38
	s_cselect_b32 s26, s33, s37
	s_cselect_b32 s24, s54, s55
	s_cselect_b32 s30, s38, s36
	s_cselect_b32 s31, s37, s33
	s_ashr_i32 s23, s22, 31
	s_lshl_b64 s[22:23], s[22:23], 19
	s_add_u32 s22, s26, s22
	s_addc_u32 s23, s25, s23
	s_and_b64 s[26:27], s[4:5], exec
	s_cselect_b32 s28, s23, s1
	s_cselect_b32 s29, s22, s0
	s_ashr_i32 s25, s24, 31
	s_lshl_b64 s[24:25], s[24:25], 19
	s_add_u32 s24, s31, s24
	s_addc_u32 s25, s30, s25
	s_and_b64 s[26:27], s[4:5], exec
	s_cselect_b32 s30, s25, s7
	s_cselect_b32 s31, s24, s6
	s_add_u32 s0, s0, 0x40080
	s_addc_u32 s1, s1, 0
	s_add_u32 s34, s6, 0x100
	s_addc_u32 s35, s7, 0
	s_mov_b32 s59, -2
	s_nop 0
	ds_read_b128 v[130:133], v163
	ds_read_b128 v[134:137], v163 offset:1024
	ds_read_b128 v[138:141], v163 offset:2048
	ds_read_b128 v[142:145], v163 offset:3072
	ds_read_b128 v[184:187], v167
	ds_read_b128 v[188:191], v167 offset:1024
	ds_read_b128 v[192:195], v167 offset:2048
	ds_read_b128 v[196:199], v167 offset:3072
	s_add_u32 s6, s0, 0xfffc0080
	s_addc_u32 s7, s1, -1
	s_cmp_eq_u32 s59, 12
	s_cselect_b32 s27, s28, s7
	s_cselect_b32 s26, s29, s6
	s_cselect_b32 s7, s30, s35
	s_cselect_b32 s6, s31, s34
	v_lshl_add_u64 v[224:225], s[0:1], 0, v[176:177]
	s_add_i32 m0, s40, 0xc000
	ds_read_b128 v[200:203], v171
	ds_read_b128 v[204:207], v171 offset:1024
	ds_read_b128 v[208:211], v171 offset:2048
	ds_read_b128 v[212:215], v171 offset:3072
	ds_read_b128 v[216:219], v171 offset:4096
	ds_read_b128 v[220:223], v171 offset:5120
	ds_read_b128 v[228:231], v171 offset:6144
	ds_read_b128 v[232:235], v171 offset:7168
	global_load_lds_dwordx4 v[224:225], off
	v_lshl_add_u64 v[224:225], s[0:1], 0, v[178:179]
	s_add_i32 m0, s40, 0xe000
	s_nop 0
	global_load_lds_dwordx4 v[224:225], off
	s_waitcnt vmcnt(8)
	s_waitcnt lgkmcnt(0)
	s_barrier
	s_setprio 1
	s_waitcnt lgkmcnt(0)
	v_mfma_i32_16x16x64_i8 v[126:129], v[130:133], v[200:203], 0
	v_mfma_i32_16x16x64_i8 v[122:125], v[138:141], v[200:203], 0
	v_mfma_i32_16x16x64_i8 v[110:113], v[130:133], v[208:211], 0
	v_mfma_i32_16x16x64_i8 v[106:109], v[138:141], v[208:211], 0
	v_mfma_i32_16x16x64_i8 v[94:97], v[130:133], v[216:219], 0
	v_mfma_i32_16x16x64_i8 v[90:93], v[138:141], v[216:219], 0
	v_mfma_i32_16x16x64_i8 v[78:81], v[130:133], v[228:231], 0
	v_mfma_i32_16x16x64_i8 v[74:77], v[138:141], v[228:231], 0
	v_mfma_i32_16x16x64_i8 v[126:129], v[134:137], v[204:207], v[126:129]
	v_mfma_i32_16x16x64_i8 v[122:125], v[142:145], v[204:207], v[122:125]
	v_mfma_i32_16x16x64_i8 v[110:113], v[134:137], v[212:215], v[110:113]
	v_mfma_i32_16x16x64_i8 v[106:109], v[142:145], v[212:215], v[106:109]
	v_mfma_i32_16x16x64_i8 v[94:97], v[134:137], v[220:223], v[94:97]
	v_mfma_i32_16x16x64_i8 v[90:93], v[142:145], v[220:223], v[90:93]
	v_mfma_i32_16x16x64_i8 v[78:81], v[134:137], v[232:235], v[78:81]
	v_mfma_i32_16x16x64_i8 v[74:77], v[142:145], v[232:235], v[74:77]
	s_setprio 0
	s_setprio 1
	v_mfma_i32_16x16x64_i8 v[118:121], v[184:187], v[200:203], 0
	v_mfma_i32_16x16x64_i8 v[114:117], v[192:195], v[200:203], 0
	v_mfma_i32_16x16x64_i8 v[102:105], v[184:187], v[208:211], 0
	v_mfma_i32_16x16x64_i8 v[98:101], v[192:195], v[208:211], 0
	v_mfma_i32_16x16x64_i8 v[86:89], v[184:187], v[216:219], 0
	v_mfma_i32_16x16x64_i8 v[82:85], v[192:195], v[216:219], 0
	v_mfma_i32_16x16x64_i8 v[70:73], v[184:187], v[228:231], 0
	v_mfma_i32_16x16x64_i8 v[66:69], v[192:195], v[228:231], 0
	v_mfma_i32_16x16x64_i8 v[118:121], v[188:191], v[204:207], v[118:121]
	v_mfma_i32_16x16x64_i8 v[114:117], v[196:199], v[204:207], v[114:117]
	v_mfma_i32_16x16x64_i8 v[102:105], v[188:191], v[212:215], v[102:105]
	v_mfma_i32_16x16x64_i8 v[98:101], v[196:199], v[212:215], v[98:101]
	v_mfma_i32_16x16x64_i8 v[86:89], v[188:191], v[220:223], v[86:89]
	v_mfma_i32_16x16x64_i8 v[82:85], v[196:199], v[220:223], v[82:85]
	v_mfma_i32_16x16x64_i8 v[70:73], v[188:191], v[232:235], v[70:73]
	v_mfma_i32_16x16x64_i8 v[66:69], v[196:199], v[232:235], v[66:69]
	s_setprio 0
	s_barrier
	s_add_i32 s60, s51, s39
	v_lshl_add_u64 v[224:225], s[6:7], 0, v[148:149]
	s_mov_b32 m0, s60
	ds_read_b128 v[200:203], v171 offset:16384
	ds_read_b128 v[204:207], v171 offset:17408
	ds_read_b128 v[208:211], v171 offset:18432
	ds_read_b128 v[212:215], v171 offset:19456
	ds_read_b128 v[216:219], v171 offset:20480
	ds_read_b128 v[220:223], v171 offset:21504
	ds_read_b128 v[228:231], v171 offset:22528
	ds_read_b128 v[232:235], v171 offset:23552
	global_load_lds_dwordx4 v[224:225], off
	s_add_i32 m0, s60, 0x2000
	s_add_u32 s60, s6, 0x40000
	v_lshl_add_u64 v[236:237], s[6:7], 0, v[152:153]
	s_addc_u32 s61, s7, 0
	s_add_i32 s62, s52, s39
	global_load_lds_dwordx4 v[236:237], off
	v_lshl_add_u64 v[238:239], s[60:61], 0, v[148:149]
	s_mov_b32 m0, s62
	v_lshl_add_u64 v[240:241], s[26:27], 0, v[150:151]
	global_load_lds_dwordx4 v[238:239], off
	v_lshl_add_u64 v[238:239], s[60:61], 0, v[152:153]
	s_add_i32 m0, s62, 0x2000
	s_nop 0
	global_load_lds_dwordx4 v[238:239], off
	v_lshl_add_u64 v[238:239], s[26:27], 0, v[146:147]
	s_mov_b32 m0, s40
	s_nop 0
	global_load_lds_dwordx4 v[238:239], off
	s_mov_b32 m0, s41
	s_nop 0
	global_load_lds_dwordx4 v[240:241], off
	s_waitcnt vmcnt(8)
	s_waitcnt lgkmcnt(0)
	s_barrier
	s_setprio 1
	s_waitcnt lgkmcnt(0)
	v_mfma_i32_16x16x64_i8 v[62:65], v[130:133], v[200:203], 0
	v_mfma_i32_16x16x64_i8 v[58:61], v[138:141], v[200:203], 0
	v_mfma_i32_16x16x64_i8 v[46:49], v[130:133], v[208:211], 0
	v_mfma_i32_16x16x64_i8 v[42:45], v[138:141], v[208:211], 0
	v_mfma_i32_16x16x64_i8 v[30:33], v[130:133], v[216:219], 0
	v_mfma_i32_16x16x64_i8 v[26:29], v[138:141], v[216:219], 0
	v_mfma_i32_16x16x64_i8 v[14:17], v[130:133], v[228:231], 0
	v_mfma_i32_16x16x64_i8 v[10:13], v[138:141], v[228:231], 0
	v_mfma_i32_16x16x64_i8 v[62:65], v[134:137], v[204:207], v[62:65]
	v_mfma_i32_16x16x64_i8 v[58:61], v[142:145], v[204:207], v[58:61]
	v_mfma_i32_16x16x64_i8 v[46:49], v[134:137], v[212:215], v[46:49]
	v_mfma_i32_16x16x64_i8 v[42:45], v[142:145], v[212:215], v[42:45]
	v_mfma_i32_16x16x64_i8 v[30:33], v[134:137], v[220:223], v[30:33]
	v_mfma_i32_16x16x64_i8 v[26:29], v[142:145], v[220:223], v[26:29]
	v_mfma_i32_16x16x64_i8 v[14:17], v[134:137], v[232:235], v[14:17]
	v_mfma_i32_16x16x64_i8 v[10:13], v[142:145], v[232:235], v[10:13]
	s_setprio 0
	s_setprio 1
	v_mfma_i32_16x16x64_i8 v[54:57], v[184:187], v[200:203], 0
	v_mfma_i32_16x16x64_i8 v[50:53], v[192:195], v[200:203], 0
	v_mfma_i32_16x16x64_i8 v[38:41], v[184:187], v[208:211], 0
	v_mfma_i32_16x16x64_i8 v[34:37], v[192:195], v[208:211], 0
	v_mfma_i32_16x16x64_i8 v[22:25], v[184:187], v[216:219], 0
	v_mfma_i32_16x16x64_i8 v[18:21], v[192:195], v[216:219], 0
	v_mfma_i32_16x16x64_i8 v[6:9], v[184:187], v[228:231], 0
	v_mfma_i32_16x16x64_i8 v[2:5], v[192:195], v[228:231], 0
	v_mfma_i32_16x16x64_i8 v[54:57], v[188:191], v[204:207], v[54:57]
	v_mfma_i32_16x16x64_i8 v[50:53], v[196:199], v[204:207], v[50:53]
	v_mfma_i32_16x16x64_i8 v[38:41], v[188:191], v[212:215], v[38:41]
	v_mfma_i32_16x16x64_i8 v[34:37], v[196:199], v[212:215], v[34:37]
	v_mfma_i32_16x16x64_i8 v[22:25], v[188:191], v[220:223], v[22:25]
	v_mfma_i32_16x16x64_i8 v[18:21], v[196:199], v[220:223], v[18:21]
	v_mfma_i32_16x16x64_i8 v[6:9], v[188:191], v[232:235], v[6:9]
	v_mfma_i32_16x16x64_i8 v[2:5], v[196:199], v[232:235], v[2:5]
	s_setprio 0
	s_barrier
	s_add_i32 s60, 0, 0x18000
	v_add_u32_e32 v0, s60, v159
	s_add_i32 s61, 0, 0x1c000
	ds_read_b128 v[130:133], v0
	ds_read_b128 v[134:137], v0 offset:1024
	ds_read_b128 v[138:141], v0 offset:2048
	ds_read_b128 v[142:145], v0 offset:3072
	v_add_u32_e32 v0, s61, v159
	ds_read_b128 v[184:187], v0
	ds_read_b128 v[188:191], v0 offset:1024
	ds_read_b128 v[192:195], v0 offset:2048
	ds_read_b128 v[196:199], v0 offset:3072
	s_add_u32 s26, s26, 0x40000
	s_addc_u32 s27, s27, 0
	s_mov_b32 m0, s42
	v_lshl_add_u64 v[242:243], s[26:27], 0, v[146:147]
	ds_read_b128 v[200:203], v171 offset:32768
	ds_read_b128 v[204:207], v171 offset:33792
	ds_read_b128 v[208:211], v171 offset:34816
	ds_read_b128 v[212:215], v171 offset:35840
	ds_read_b128 v[216:219], v171 offset:36864
	ds_read_b128 v[220:223], v171 offset:37888
	ds_read_b128 v[228:231], v171 offset:38912
	ds_read_b128 v[232:235], v171 offset:39936
	global_load_lds_dwordx4 v[242:243], off
	v_lshl_add_u64 v[242:243], s[26:27], 0, v[150:151]
	s_mov_b32 m0, s43
	s_nop 0
	global_load_lds_dwordx4 v[242:243], off
	s_waitcnt vmcnt(8)
	s_waitcnt lgkmcnt(0)
	s_barrier
	s_setprio 1
	s_waitcnt lgkmcnt(0)
	v_mfma_i32_16x16x64_i8 v[126:129], v[130:133], v[200:203], v[126:129]
	v_mfma_i32_16x16x64_i8 v[122:125], v[138:141], v[200:203], v[122:125]
	v_mfma_i32_16x16x64_i8 v[110:113], v[130:133], v[208:211], v[110:113]
	v_mfma_i32_16x16x64_i8 v[106:109], v[138:141], v[208:211], v[106:109]
	v_mfma_i32_16x16x64_i8 v[94:97], v[130:133], v[216:219], v[94:97]
	v_mfma_i32_16x16x64_i8 v[90:93], v[138:141], v[216:219], v[90:93]
	v_mfma_i32_16x16x64_i8 v[78:81], v[130:133], v[228:231], v[78:81]
	v_mfma_i32_16x16x64_i8 v[74:77], v[138:141], v[228:231], v[74:77]
	v_mfma_i32_16x16x64_i8 v[126:129], v[134:137], v[204:207], v[126:129]
	v_mfma_i32_16x16x64_i8 v[122:125], v[142:145], v[204:207], v[122:125]
	v_mfma_i32_16x16x64_i8 v[110:113], v[134:137], v[212:215], v[110:113]
	v_mfma_i32_16x16x64_i8 v[106:109], v[142:145], v[212:215], v[106:109]
	v_mfma_i32_16x16x64_i8 v[94:97], v[134:137], v[220:223], v[94:97]
	v_mfma_i32_16x16x64_i8 v[90:93], v[142:145], v[220:223], v[90:93]
	v_mfma_i32_16x16x64_i8 v[78:81], v[134:137], v[232:235], v[78:81]
	v_mfma_i32_16x16x64_i8 v[74:77], v[142:145], v[232:235], v[74:77]
	s_setprio 0
	s_setprio 1
	v_mfma_i32_16x16x64_i8 v[118:121], v[184:187], v[200:203], v[118:121]
	v_mfma_i32_16x16x64_i8 v[114:117], v[192:195], v[200:203], v[114:117]
	v_mfma_i32_16x16x64_i8 v[102:105], v[184:187], v[208:211], v[102:105]
	v_mfma_i32_16x16x64_i8 v[98:101], v[192:195], v[208:211], v[98:101]
	v_mfma_i32_16x16x64_i8 v[86:89], v[184:187], v[216:219], v[86:89]
	v_mfma_i32_16x16x64_i8 v[82:85], v[192:195], v[216:219], v[82:85]
	v_mfma_i32_16x16x64_i8 v[70:73], v[184:187], v[228:231], v[70:73]
	v_mfma_i32_16x16x64_i8 v[66:69], v[192:195], v[228:231], v[66:69]
	v_mfma_i32_16x16x64_i8 v[118:121], v[188:191], v[204:207], v[118:121]
	v_mfma_i32_16x16x64_i8 v[114:117], v[196:199], v[204:207], v[114:117]
	v_mfma_i32_16x16x64_i8 v[102:105], v[188:191], v[212:215], v[102:105]
	v_mfma_i32_16x16x64_i8 v[98:101], v[196:199], v[212:215], v[98:101]
	v_mfma_i32_16x16x64_i8 v[86:89], v[188:191], v[220:223], v[86:89]
	v_mfma_i32_16x16x64_i8 v[82:85], v[196:199], v[220:223], v[82:85]
	v_mfma_i32_16x16x64_i8 v[70:73], v[188:191], v[232:235], v[70:73]
	v_mfma_i32_16x16x64_i8 v[66:69], v[196:199], v[232:235], v[66:69]
	s_setprio 0
	s_barrier
	s_add_i32 s26, s60, s39
	v_lshl_add_u64 v[224:225], v[224:225], 0, s[12:13]
	s_mov_b32 m0, s26
	ds_read_b128 v[200:203], v171 offset:49152
	ds_read_b128 v[204:207], v171 offset:50176
	ds_read_b128 v[208:211], v171 offset:51200
	ds_read_b128 v[212:215], v171 offset:52224
	ds_read_b128 v[216:219], v171 offset:53248
	ds_read_b128 v[220:223], v171 offset:54272
	ds_read_b128 v[228:231], v171 offset:55296
	ds_read_b128 v[232:235], v171 offset:56320
	global_load_lds_dwordx4 v[224:225], off
	s_add_i32 m0, s26, 0x2000
	s_add_u32 s6, s6, 0x40080
	v_lshl_add_u64 v[224:225], v[236:237], 0, s[12:13]
	s_addc_u32 s7, s7, 0
	s_add_i32 s26, s61, s39
	global_load_lds_dwordx4 v[224:225], off
	v_lshl_add_u64 v[224:225], s[6:7], 0, v[148:149]
	s_mov_b32 m0, s26
	s_nop 0
	global_load_lds_dwordx4 v[224:225], off
	v_lshl_add_u64 v[224:225], s[6:7], 0, v[152:153]
	s_add_i32 m0, s26, 0x2000
	s_nop 0
	global_load_lds_dwordx4 v[224:225], off
	v_lshl_add_u64 v[224:225], v[238:239], 0, s[12:13]
	s_mov_b32 m0, s45
	s_nop 0
	global_load_lds_dwordx4 v[224:225], off
	v_lshl_add_u64 v[224:225], v[240:241], 0, s[12:13]
	s_mov_b32 m0, s46
	s_nop 0
	global_load_lds_dwordx4 v[224:225], off
	s_waitcnt vmcnt(8)
	s_waitcnt lgkmcnt(0)
	s_barrier
	s_setprio 1
	s_waitcnt lgkmcnt(0)
	v_mfma_i32_16x16x64_i8 v[62:65], v[130:133], v[200:203], v[62:65]
	v_mfma_i32_16x16x64_i8 v[58:61], v[138:141], v[200:203], v[58:61]
	v_mfma_i32_16x16x64_i8 v[46:49], v[130:133], v[208:211], v[46:49]
	v_mfma_i32_16x16x64_i8 v[42:45], v[138:141], v[208:211], v[42:45]
	v_mfma_i32_16x16x64_i8 v[30:33], v[130:133], v[216:219], v[30:33]
	v_mfma_i32_16x16x64_i8 v[26:29], v[138:141], v[216:219], v[26:29]
	v_mfma_i32_16x16x64_i8 v[14:17], v[130:133], v[228:231], v[14:17]
	v_mfma_i32_16x16x64_i8 v[10:13], v[138:141], v[228:231], v[10:13]
	v_mfma_i32_16x16x64_i8 v[62:65], v[134:137], v[204:207], v[62:65]
	v_mfma_i32_16x16x64_i8 v[58:61], v[142:145], v[204:207], v[58:61]
	v_mfma_i32_16x16x64_i8 v[46:49], v[134:137], v[212:215], v[46:49]
	v_mfma_i32_16x16x64_i8 v[42:45], v[142:145], v[212:215], v[42:45]
	v_mfma_i32_16x16x64_i8 v[30:33], v[134:137], v[220:223], v[30:33]
	v_mfma_i32_16x16x64_i8 v[26:29], v[142:145], v[220:223], v[26:29]
	v_mfma_i32_16x16x64_i8 v[14:17], v[134:137], v[232:235], v[14:17]
	v_mfma_i32_16x16x64_i8 v[10:13], v[142:145], v[232:235], v[10:13]
	s_setprio 0
	s_setprio 1
	v_mfma_i32_16x16x64_i8 v[54:57], v[184:187], v[200:203], v[54:57]
	v_mfma_i32_16x16x64_i8 v[50:53], v[192:195], v[200:203], v[50:53]
	v_mfma_i32_16x16x64_i8 v[38:41], v[184:187], v[208:211], v[38:41]
	v_mfma_i32_16x16x64_i8 v[34:37], v[192:195], v[208:211], v[34:37]
	v_mfma_i32_16x16x64_i8 v[22:25], v[184:187], v[216:219], v[22:25]
	v_mfma_i32_16x16x64_i8 v[18:21], v[192:195], v[216:219], v[18:21]
	v_mfma_i32_16x16x64_i8 v[6:9], v[184:187], v[228:231], v[6:9]
	v_mfma_i32_16x16x64_i8 v[2:5], v[192:195], v[228:231], v[2:5]
	v_mfma_i32_16x16x64_i8 v[54:57], v[188:191], v[204:207], v[54:57]
	v_mfma_i32_16x16x64_i8 v[50:53], v[196:199], v[204:207], v[50:53]
	v_mfma_i32_16x16x64_i8 v[38:41], v[188:191], v[212:215], v[38:41]
	v_mfma_i32_16x16x64_i8 v[34:37], v[196:199], v[212:215], v[34:37]
	v_mfma_i32_16x16x64_i8 v[22:25], v[188:191], v[220:223], v[22:25]
	v_mfma_i32_16x16x64_i8 v[18:21], v[196:199], v[220:223], v[18:21]
	v_mfma_i32_16x16x64_i8 v[6:9], v[188:191], v[232:235], v[6:9]
	v_mfma_i32_16x16x64_i8 v[2:5], v[196:199], v[232:235], v[2:5]
	s_setprio 0
	s_barrier
	s_add_i32 s59, s59, 2
	s_add_u32 s0, s0, 0x100
	s_addc_u32 s1, s1, 0
	s_add_u32 s34, s34, 0x100
	s_addc_u32 s35, s35, 0
	s_cmp_gt_u32 s59, 13
	s_cbranch_scc0 .LBB0_162
	s_branch .Lkexit_162
	s_nop 0
	s_nop 0
	s_nop 0
	s_nop 0
	s_nop 0
	s_nop 0
	s_nop 0
	s_nop 0

.LBB0_981:
	s_ashr_i32 s11, s10, 31
	s_lshl_b64 s[12:13], s[10:11], 20
	s_add_u32 s12, s24, s12
	s_addc_u32 s13, s25, s13
	s_and_b64 s[14:15], s[4:5], exec
	s_cselect_b32 s11, s13, s19
	s_cselect_b32 s41, s12, s18
	s_ashr_i32 s9, s8, 31
	s_lshl_b64 s[14:15], s[8:9], 20
	s_add_u32 s14, s27, s14
	s_addc_u32 s15, s28, s15
	s_and_b64 s[22:23], s[4:5], exec
	s_cselect_b32 s9, s15, s21
	s_cselect_b32 s42, s14, s20
	s_add_u32 s18, s18, 0x80080
	s_addc_u32 s19, s19, 0
	s_add_u32 s43, s20, 0x100
	s_addc_u32 s44, s21, 0
	s_mov_b32 s45, -2
	ds_read_b128 v[146:149], v154
	ds_read_b128 v[158:161], v154 offset:1024
	ds_read_b128 v[162:165], v154 offset:2048
	ds_read_b128 v[166:169], v154 offset:3072
	ds_read_b128 v[170:173], v155
	ds_read_b128 v[174:177], v155 offset:1024
	ds_read_b128 v[178:181], v155 offset:2048
	ds_read_b128 v[182:185], v155 offset:3072
	s_add_u32 s20, s18, 0xfff80080
	s_addc_u32 s21, s19, -1
	s_cmp_eq_u32 s45, 28
	s_cselect_b32 s23, s11, s21
	s_cselect_b32 s22, s41, s20
	s_cselect_b32 s21, s9, s44
	s_cselect_b32 s20, s42, s43
	v_lshl_add_u64 v[150:151], s[18:19], 0, v[138:139]
	s_add_i32 m0, s17, 0xc000
	ds_read_b128 v[186:189], v156
	ds_read_b128 v[190:193], v156 offset:1024
	ds_read_b128 v[194:197], v156 offset:2048
	ds_read_b128 v[198:201], v156 offset:3072
	ds_read_b128 v[202:205], v156 offset:4096
	ds_read_b128 v[206:209], v156 offset:5120
	ds_read_b128 v[210:213], v156 offset:6144
	ds_read_b128 v[214:217], v156 offset:7168
	global_load_lds_dwordx4 v[150:151], off
	v_lshl_add_u64 v[150:151], s[18:19], 0, v[140:141]
	s_add_i32 m0, s17, 0xe000
	s_nop 0
	global_load_lds_dwordx4 v[150:151], off
	s_waitcnt vmcnt(40)
	s_waitcnt lgkmcnt(0)
	s_barrier
	s_setprio 1
	s_waitcnt lgkmcnt(0)
	v_mfma_f32_16x16x32_bf16 v[126:129], v[146:149], v[186:189], 0
	v_mfma_f32_16x16x32_bf16 v[122:125], v[162:165], v[186:189], 0
	v_mfma_f32_16x16x32_bf16 v[118:121], v[146:149], v[194:197], 0
	v_mfma_f32_16x16x32_bf16 v[114:117], v[162:165], v[194:197], 0
	v_mfma_f32_16x16x32_bf16 v[106:109], v[146:149], v[202:205], 0
	v_mfma_f32_16x16x32_bf16 v[98:101], v[162:165], v[202:205], 0
	v_mfma_f32_16x16x32_bf16 v[86:89], v[146:149], v[210:213], 0
	v_mfma_f32_16x16x32_bf16 v[78:81], v[162:165], v[210:213], 0
	v_mfma_f32_16x16x32_bf16 v[126:129], v[158:161], v[190:193], v[126:129]
	v_mfma_f32_16x16x32_bf16 v[122:125], v[166:169], v[190:193], v[122:125]
	v_mfma_f32_16x16x32_bf16 v[118:121], v[158:161], v[198:201], v[118:121]
	v_mfma_f32_16x16x32_bf16 v[114:117], v[166:169], v[198:201], v[114:117]
	v_mfma_f32_16x16x32_bf16 v[106:109], v[158:161], v[206:209], v[106:109]
	v_mfma_f32_16x16x32_bf16 v[98:101], v[166:169], v[206:209], v[98:101]
	v_mfma_f32_16x16x32_bf16 v[86:89], v[158:161], v[214:217], v[86:89]
	v_mfma_f32_16x16x32_bf16 v[78:81], v[166:169], v[214:217], v[78:81]
	s_setprio 0
	s_setprio 1
	v_mfma_f32_16x16x32_bf16 v[110:113], v[170:173], v[186:189], 0
	v_mfma_f32_16x16x32_bf16 v[102:105], v[178:181], v[186:189], 0
	v_mfma_f32_16x16x32_bf16 v[94:97], v[170:173], v[194:197], 0
	v_mfma_f32_16x16x32_bf16 v[90:93], v[178:181], v[194:197], 0
	v_mfma_f32_16x16x32_bf16 v[82:85], v[170:173], v[202:205], 0
	v_mfma_f32_16x16x32_bf16 v[74:77], v[178:181], v[202:205], 0
	v_mfma_f32_16x16x32_bf16 v[70:73], v[170:173], v[210:213], 0
	v_mfma_f32_16x16x32_bf16 v[66:69], v[178:181], v[210:213], 0
	v_mfma_f32_16x16x32_bf16 v[110:113], v[174:177], v[190:193], v[110:113]
	v_mfma_f32_16x16x32_bf16 v[102:105], v[182:185], v[190:193], v[102:105]
	v_mfma_f32_16x16x32_bf16 v[94:97], v[174:177], v[198:201], v[94:97]
	v_mfma_f32_16x16x32_bf16 v[90:93], v[182:185], v[198:201], v[90:93]
	v_mfma_f32_16x16x32_bf16 v[82:85], v[174:177], v[206:209], v[82:85]
	v_mfma_f32_16x16x32_bf16 v[74:77], v[182:185], v[206:209], v[74:77]
	v_mfma_f32_16x16x32_bf16 v[70:73], v[174:177], v[214:217], v[70:73]
	v_mfma_f32_16x16x32_bf16 v[66:69], v[182:185], v[214:217], v[66:69]
	s_setprio 0
	s_barrier
	s_add_i32 s46, s38, s29
	v_lshl_add_u64 v[150:151], s[20:21], 0, v[132:133]
	s_mov_b32 m0, s46
	ds_read_b128 v[186:189], v156 offset:16384
	ds_read_b128 v[190:193], v156 offset:17408
	ds_read_b128 v[194:197], v156 offset:18432
	ds_read_b128 v[198:201], v156 offset:19456
	ds_read_b128 v[202:205], v156 offset:20480
	ds_read_b128 v[206:209], v156 offset:21504
	ds_read_b128 v[210:213], v156 offset:22528
	ds_read_b128 v[214:217], v156 offset:23552
	global_load_lds_dwordx4 v[150:151], off
	s_add_i32 m0, s46, 0x2000
	s_add_u32 s46, s20, 0x80000
	v_lshl_add_u64 v[218:219], s[20:21], 0, v[136:137]
	s_addc_u32 s47, s21, 0
	s_add_i32 s48, s39, s29
	global_load_lds_dwordx4 v[218:219], off
	v_lshl_add_u64 v[220:221], s[46:47], 0, v[132:133]
	s_mov_b32 m0, s48
	v_lshl_add_u64 v[222:223], s[22:23], 0, v[134:135]
	global_load_lds_dwordx4 v[220:221], off
	v_lshl_add_u64 v[220:221], s[46:47], 0, v[136:137]
	s_add_i32 m0, s48, 0x2000
	s_nop 0
	global_load_lds_dwordx4 v[220:221], off
	v_lshl_add_u64 v[220:221], s[22:23], 0, v[130:131]
	s_mov_b32 m0, s17
	s_nop 0
	global_load_lds_dwordx4 v[220:221], off
	s_mov_b32 m0, s30
	s_nop 0
	global_load_lds_dwordx4 v[222:223], off
	s_waitcnt vmcnt(8)
	s_waitcnt lgkmcnt(0)
	s_barrier
	s_setprio 1
	s_waitcnt lgkmcnt(0)
	v_mfma_f32_16x16x32_bf16 v[62:65], v[146:149], v[186:189], 0
	v_mfma_f32_16x16x32_bf16 v[58:61], v[162:165], v[186:189], 0
	v_mfma_f32_16x16x32_bf16 v[50:53], v[146:149], v[194:197], 0
	v_mfma_f32_16x16x32_bf16 v[42:45], v[162:165], v[194:197], 0
	v_mfma_f32_16x16x32_bf16 v[38:41], v[146:149], v[202:205], 0
	v_mfma_f32_16x16x32_bf16 v[30:33], v[162:165], v[202:205], 0
	v_mfma_f32_16x16x32_bf16 v[22:25], v[146:149], v[210:213], 0
	v_mfma_f32_16x16x32_bf16 v[14:17], v[162:165], v[210:213], 0
	v_mfma_f32_16x16x32_bf16 v[62:65], v[158:161], v[190:193], v[62:65]
	v_mfma_f32_16x16x32_bf16 v[58:61], v[166:169], v[190:193], v[58:61]
	v_mfma_f32_16x16x32_bf16 v[50:53], v[158:161], v[198:201], v[50:53]
	v_mfma_f32_16x16x32_bf16 v[42:45], v[166:169], v[198:201], v[42:45]
	v_mfma_f32_16x16x32_bf16 v[38:41], v[158:161], v[206:209], v[38:41]
	v_mfma_f32_16x16x32_bf16 v[30:33], v[166:169], v[206:209], v[30:33]
	v_mfma_f32_16x16x32_bf16 v[22:25], v[158:161], v[214:217], v[22:25]
	v_mfma_f32_16x16x32_bf16 v[14:17], v[166:169], v[214:217], v[14:17]
	s_setprio 0
	s_setprio 1
	v_mfma_f32_16x16x32_bf16 v[54:57], v[170:173], v[186:189], 0
	v_mfma_f32_16x16x32_bf16 v[46:49], v[178:181], v[186:189], 0
	v_mfma_f32_16x16x32_bf16 v[34:37], v[170:173], v[194:197], 0
	v_mfma_f32_16x16x32_bf16 v[26:29], v[178:181], v[194:197], 0
	v_mfma_f32_16x16x32_bf16 v[18:21], v[170:173], v[202:205], 0
	v_mfma_f32_16x16x32_bf16 v[10:13], v[178:181], v[202:205], 0
	v_mfma_f32_16x16x32_bf16 v[6:9], v[170:173], v[210:213], 0
	v_mfma_f32_16x16x32_bf16 v[2:5], v[178:181], v[210:213], 0
	v_mfma_f32_16x16x32_bf16 v[54:57], v[174:177], v[190:193], v[54:57]
	v_mfma_f32_16x16x32_bf16 v[46:49], v[182:185], v[190:193], v[46:49]
	v_mfma_f32_16x16x32_bf16 v[34:37], v[174:177], v[198:201], v[34:37]
	v_mfma_f32_16x16x32_bf16 v[26:29], v[182:185], v[198:201], v[26:29]
	v_mfma_f32_16x16x32_bf16 v[18:21], v[174:177], v[206:209], v[18:21]
	v_mfma_f32_16x16x32_bf16 v[10:13], v[182:185], v[206:209], v[10:13]
	v_mfma_f32_16x16x32_bf16 v[6:9], v[174:177], v[214:217], v[6:9]
	v_mfma_f32_16x16x32_bf16 v[2:5], v[182:185], v[214:217], v[2:5]
	s_setprio 0
	s_barrier
	s_add_i32 s46, 0, 0x18000
	v_add_u32_e32 v0, s46, v152
	s_add_i32 s47, 0, 0x1c000
	ds_read_b128 v[146:149], v0
	ds_read_b128 v[158:161], v0 offset:1024
	ds_read_b128 v[162:165], v0 offset:2048
	ds_read_b128 v[166:169], v0 offset:3072
	v_add_u32_e32 v0, s47, v152
	ds_read_b128 v[170:173], v0
	ds_read_b128 v[174:177], v0 offset:1024
	ds_read_b128 v[178:181], v0 offset:2048
	ds_read_b128 v[182:185], v0 offset:3072
	s_add_u32 s22, s22, 0x80000
	s_addc_u32 s23, s23, 0
	s_mov_b32 m0, s31
	v_lshl_add_u64 v[224:225], s[22:23], 0, v[130:131]
	ds_read_b128 v[186:189], v156 offset:32768
	ds_read_b128 v[190:193], v156 offset:33792
	ds_read_b128 v[194:197], v156 offset:34816
	ds_read_b128 v[198:201], v156 offset:35840
	ds_read_b128 v[202:205], v156 offset:36864
	ds_read_b128 v[206:209], v156 offset:37888
	ds_read_b128 v[210:213], v156 offset:38912
	ds_read_b128 v[214:217], v156 offset:39936
	global_load_lds_dwordx4 v[224:225], off
	v_lshl_add_u64 v[224:225], s[22:23], 0, v[134:135]
	s_mov_b32 m0, s33
	s_nop 0
	global_load_lds_dwordx4 v[224:225], off
	s_waitcnt vmcnt(8)
	s_waitcnt lgkmcnt(0)
	s_barrier
	s_setprio 1
	s_waitcnt lgkmcnt(0)
	v_mfma_f32_16x16x32_bf16 v[126:129], v[146:149], v[186:189], v[126:129]
	v_mfma_f32_16x16x32_bf16 v[122:125], v[162:165], v[186:189], v[122:125]
	v_mfma_f32_16x16x32_bf16 v[118:121], v[146:149], v[194:197], v[118:121]
	v_mfma_f32_16x16x32_bf16 v[114:117], v[162:165], v[194:197], v[114:117]
	v_mfma_f32_16x16x32_bf16 v[106:109], v[146:149], v[202:205], v[106:109]
	v_mfma_f32_16x16x32_bf16 v[98:101], v[162:165], v[202:205], v[98:101]
	v_mfma_f32_16x16x32_bf16 v[86:89], v[146:149], v[210:213], v[86:89]
	v_mfma_f32_16x16x32_bf16 v[78:81], v[162:165], v[210:213], v[78:81]
	v_mfma_f32_16x16x32_bf16 v[126:129], v[158:161], v[190:193], v[126:129]
	v_mfma_f32_16x16x32_bf16 v[122:125], v[166:169], v[190:193], v[122:125]
	v_mfma_f32_16x16x32_bf16 v[118:121], v[158:161], v[198:201], v[118:121]
	v_mfma_f32_16x16x32_bf16 v[114:117], v[166:169], v[198:201], v[114:117]
	v_mfma_f32_16x16x32_bf16 v[106:109], v[158:161], v[206:209], v[106:109]
	v_mfma_f32_16x16x32_bf16 v[98:101], v[166:169], v[206:209], v[98:101]
	v_mfma_f32_16x16x32_bf16 v[86:89], v[158:161], v[214:217], v[86:89]
	v_mfma_f32_16x16x32_bf16 v[78:81], v[166:169], v[214:217], v[78:81]
	s_setprio 0
	s_setprio 1
	v_mfma_f32_16x16x32_bf16 v[110:113], v[170:173], v[186:189], v[110:113]
	v_mfma_f32_16x16x32_bf16 v[102:105], v[178:181], v[186:189], v[102:105]
	v_mfma_f32_16x16x32_bf16 v[94:97], v[170:173], v[194:197], v[94:97]
	v_mfma_f32_16x16x32_bf16 v[90:93], v[178:181], v[194:197], v[90:93]
	v_mfma_f32_16x16x32_bf16 v[82:85], v[170:173], v[202:205], v[82:85]
	v_mfma_f32_16x16x32_bf16 v[74:77], v[178:181], v[202:205], v[74:77]
	v_mfma_f32_16x16x32_bf16 v[70:73], v[170:173], v[210:213], v[70:73]
	v_mfma_f32_16x16x32_bf16 v[66:69], v[178:181], v[210:213], v[66:69]
	v_mfma_f32_16x16x32_bf16 v[110:113], v[174:177], v[190:193], v[110:113]
	v_mfma_f32_16x16x32_bf16 v[102:105], v[182:185], v[190:193], v[102:105]
	v_mfma_f32_16x16x32_bf16 v[94:97], v[174:177], v[198:201], v[94:97]
	v_mfma_f32_16x16x32_bf16 v[90:93], v[182:185], v[198:201], v[90:93]
	v_mfma_f32_16x16x32_bf16 v[82:85], v[174:177], v[206:209], v[82:85]
	v_mfma_f32_16x16x32_bf16 v[74:77], v[182:185], v[206:209], v[74:77]
	v_mfma_f32_16x16x32_bf16 v[70:73], v[174:177], v[214:217], v[70:73]
	v_mfma_f32_16x16x32_bf16 v[66:69], v[182:185], v[214:217], v[66:69]
	s_setprio 0
	s_barrier
	s_add_i32 s22, s46, s29
	v_lshl_add_u64 v[150:151], v[150:151], 0, s[2:3]
	s_mov_b32 m0, s22
	ds_read_b128 v[186:189], v156 offset:49152
	ds_read_b128 v[190:193], v156 offset:50176
	ds_read_b128 v[194:197], v156 offset:51200
	ds_read_b128 v[198:201], v156 offset:52224
	ds_read_b128 v[202:205], v156 offset:53248
	ds_read_b128 v[206:209], v156 offset:54272
	ds_read_b128 v[210:213], v156 offset:55296
	ds_read_b128 v[214:217], v156 offset:56320
	global_load_lds_dwordx4 v[150:151], off
	s_add_i32 m0, s22, 0x2000
	s_add_u32 s20, s20, 0x80080
	v_lshl_add_u64 v[150:151], v[218:219], 0, s[2:3]
	s_addc_u32 s21, s21, 0
	s_add_i32 s22, s47, s29
	global_load_lds_dwordx4 v[150:151], off
	v_lshl_add_u64 v[150:151], s[20:21], 0, v[132:133]
	s_mov_b32 m0, s22
	s_nop 0
	global_load_lds_dwordx4 v[150:151], off
	v_lshl_add_u64 v[150:151], s[20:21], 0, v[136:137]
	s_add_i32 m0, s22, 0x2000
	s_nop 0
	global_load_lds_dwordx4 v[150:151], off
	v_lshl_add_u64 v[150:151], v[220:221], 0, s[2:3]
	s_mov_b32 m0, s35
	s_nop 0
	global_load_lds_dwordx4 v[150:151], off
	v_lshl_add_u64 v[150:151], v[222:223], 0, s[2:3]
	s_mov_b32 m0, s36
	s_nop 0
	global_load_lds_dwordx4 v[150:151], off
	s_waitcnt vmcnt(8)
	s_waitcnt lgkmcnt(0)
	s_barrier
	s_setprio 1
	s_waitcnt lgkmcnt(0)
	v_mfma_f32_16x16x32_bf16 v[62:65], v[146:149], v[186:189], v[62:65]
	v_mfma_f32_16x16x32_bf16 v[58:61], v[162:165], v[186:189], v[58:61]
	v_mfma_f32_16x16x32_bf16 v[50:53], v[146:149], v[194:197], v[50:53]
	v_mfma_f32_16x16x32_bf16 v[42:45], v[162:165], v[194:197], v[42:45]
	v_mfma_f32_16x16x32_bf16 v[38:41], v[146:149], v[202:205], v[38:41]
	v_mfma_f32_16x16x32_bf16 v[30:33], v[162:165], v[202:205], v[30:33]
	v_mfma_f32_16x16x32_bf16 v[22:25], v[146:149], v[210:213], v[22:25]
	v_mfma_f32_16x16x32_bf16 v[14:17], v[162:165], v[210:213], v[14:17]
	v_mfma_f32_16x16x32_bf16 v[62:65], v[158:161], v[190:193], v[62:65]
	v_mfma_f32_16x16x32_bf16 v[58:61], v[166:169], v[190:193], v[58:61]
	v_mfma_f32_16x16x32_bf16 v[50:53], v[158:161], v[198:201], v[50:53]
	v_mfma_f32_16x16x32_bf16 v[42:45], v[166:169], v[198:201], v[42:45]
	v_mfma_f32_16x16x32_bf16 v[38:41], v[158:161], v[206:209], v[38:41]
	v_mfma_f32_16x16x32_bf16 v[30:33], v[166:169], v[206:209], v[30:33]
	v_mfma_f32_16x16x32_bf16 v[22:25], v[158:161], v[214:217], v[22:25]
	v_mfma_f32_16x16x32_bf16 v[14:17], v[166:169], v[214:217], v[14:17]
	s_setprio 0
	s_setprio 1
	v_mfma_f32_16x16x32_bf16 v[54:57], v[170:173], v[186:189], v[54:57]
	v_mfma_f32_16x16x32_bf16 v[46:49], v[178:181], v[186:189], v[46:49]
	v_mfma_f32_16x16x32_bf16 v[34:37], v[170:173], v[194:197], v[34:37]
	v_mfma_f32_16x16x32_bf16 v[26:29], v[178:181], v[194:197], v[26:29]
	v_mfma_f32_16x16x32_bf16 v[18:21], v[170:173], v[202:205], v[18:21]
	v_mfma_f32_16x16x32_bf16 v[10:13], v[178:181], v[202:205], v[10:13]
	v_mfma_f32_16x16x32_bf16 v[6:9], v[170:173], v[210:213], v[6:9]
	v_mfma_f32_16x16x32_bf16 v[2:5], v[178:181], v[210:213], v[2:5]
	v_mfma_f32_16x16x32_bf16 v[54:57], v[174:177], v[190:193], v[54:57]
	v_mfma_f32_16x16x32_bf16 v[46:49], v[182:185], v[190:193], v[46:49]
	v_mfma_f32_16x16x32_bf16 v[34:37], v[174:177], v[198:201], v[34:37]
	v_mfma_f32_16x16x32_bf16 v[26:29], v[182:185], v[198:201], v[26:29]
	v_mfma_f32_16x16x32_bf16 v[18:21], v[174:177], v[206:209], v[18:21]
	v_mfma_f32_16x16x32_bf16 v[10:13], v[182:185], v[206:209], v[10:13]
	v_mfma_f32_16x16x32_bf16 v[6:9], v[174:177], v[214:217], v[6:9]
	v_mfma_f32_16x16x32_bf16 v[2:5], v[182:185], v[214:217], v[2:5]
	s_setprio 0
	s_barrier
	s_add_i32 s45, s45, 2
	s_add_u32 s18, s18, 0x100
	s_addc_u32 s19, s19, 0
	s_add_u32 s43, s43, 0x100
	s_addc_u32 s44, s44, 0
	s_cmp_gt_u32 s45, 29
	s_cbranch_scc0 .LBB0_982
	s_branch .Lkexit_982
	s_nop 0
	s_nop 0
	s_nop 0
	s_nop 0
	s_nop 0
	s_nop 0
	s_nop 0
	s_nop 0

.LBB0_1213:
	s_add_u32 s35, s42, 0x100
	s_addc_u32 s37, s43, 0
	s_mov_b32 s39, -2
	s_mov_b64 s[42:43], 0
	ds_read_b128 v[70:73], v190
	ds_read_b128 v[74:77], v190 offset:1024
	ds_read_b128 v[78:81], v190 offset:2048
	ds_read_b128 v[82:85], v190 offset:3072
	ds_read_b128 v[94:97], v191
	ds_read_b128 v[98:101], v191 offset:1024
	ds_read_b128 v[102:105], v191 offset:2048
	ds_read_b128 v[106:109], v191 offset:3072
	s_add_u32 s44, s42, 0x100
	s_addc_u32 s45, s43, 0
	s_add_u32 s48, s35, s42
	s_addc_u32 s49, s37, s43
	s_cmp_eq_u32 s39, 12
	s_cselect_b64 vcc, -1, 0
	s_and_b64 s[46:47], vcc, exec
	s_cselect_b32 s73, 0, s44
	s_cselect_b32 s72, 0, s45
	s_cselect_b32 s46, s0, s48
	s_cselect_b32 s47, s1, s49
	s_add_u32 s48, s14, s73
	s_addc_u32 s49, s15, s72
	s_add_i32 m0, s11, 0xc000
	s_add_u32 s42, s24, s42
	s_addc_u32 s43, s25, s43
	ds_read_b128 v[176:179], v192
	ds_read_b128 v[180:183], v192 offset:1024
	ds_read_b128 v[194:197], v192 offset:2048
	ds_read_b128 v[198:201], v192 offset:3072
	ds_read_b128 v[202:205], v192 offset:4096
	ds_read_b128 v[206:209], v192 offset:5120
	ds_read_b128 v[210:213], v192 offset:6144
	ds_read_b128 v[214:217], v192 offset:7168
	global_load_lds_dwordx4 v187, s[42:43]
	s_add_i32 m0, s11, 0xe000
	v_mov_b32_e32 v0, v172
	global_load_lds_dwordx4 v186, s[42:43]
	v_mov_b32_e32 v169, v173
	v_lshlrev_b32_e32 v184, 11, v0
	v_lshlrev_b32_e32 v185, 11, v169
	v_bfe_u32 v0, v0, 16, 16
	v_bfe_u32 v169, v169, 16, 16
	v_and_b32_e32 v184, 0x7fff800, v184
	v_and_b32_e32 v185, 0x7fff800, v185
	v_lshl_add_u32 v0, v0, 11, v175
	v_lshl_add_u32 v169, v169, 11, v175
	v_add_u32_e32 v184, v184, v175
	v_add_u32_e32 v185, v185, v175
	v_cndmask_b32_e32 v168, v168, v0, vcc
	v_cndmask_b32_e32 v186, v186, v169, vcc
	v_cndmask_b32_e32 v170, v170, v184, vcc
	v_cndmask_b32_e32 v187, v187, v185, vcc
	s_waitcnt vmcnt(24)
	s_waitcnt lgkmcnt(0)
	s_barrier
	s_setprio 1
	s_waitcnt lgkmcnt(0)
	v_mfma_i32_16x16x64_i8 v[158:161], v[70:73], v[176:179], 0
	v_mfma_i32_16x16x64_i8 v[150:153], v[78:81], v[176:179], 0
	v_mfma_i32_16x16x64_i8 v[142:145], v[70:73], v[194:197], 0
	v_mfma_i32_16x16x64_i8 v[134:137], v[78:81], v[194:197], 0
	v_mfma_i32_16x16x64_i8 v[126:129], v[70:73], v[202:205], 0
	v_mfma_i32_16x16x64_i8 v[118:121], v[78:81], v[202:205], 0
	v_mfma_i32_16x16x64_i8 v[110:113], v[70:73], v[210:213], 0
	v_mfma_i32_16x16x64_i8 v[86:89], v[78:81], v[210:213], 0
	v_mfma_i32_16x16x64_i8 v[158:161], v[74:77], v[180:183], v[158:161]
	v_mfma_i32_16x16x64_i8 v[150:153], v[82:85], v[180:183], v[150:153]
	v_mfma_i32_16x16x64_i8 v[142:145], v[74:77], v[198:201], v[142:145]
	v_mfma_i32_16x16x64_i8 v[134:137], v[82:85], v[198:201], v[134:137]
	v_mfma_i32_16x16x64_i8 v[126:129], v[74:77], v[206:209], v[126:129]
	v_mfma_i32_16x16x64_i8 v[118:121], v[82:85], v[206:209], v[118:121]
	v_mfma_i32_16x16x64_i8 v[110:113], v[74:77], v[214:217], v[110:113]
	v_mfma_i32_16x16x64_i8 v[86:89], v[82:85], v[214:217], v[86:89]
	s_setprio 0
	s_setprio 1
	v_mfma_i32_16x16x64_i8 v[154:157], v[94:97], v[176:179], 0
	v_mfma_i32_16x16x64_i8 v[146:149], v[102:105], v[176:179], 0
	v_mfma_i32_16x16x64_i8 v[138:141], v[94:97], v[194:197], 0
	v_mfma_i32_16x16x64_i8 v[130:133], v[102:105], v[194:197], 0
	v_mfma_i32_16x16x64_i8 v[122:125], v[94:97], v[202:205], 0
	v_mfma_i32_16x16x64_i8 v[114:117], v[102:105], v[202:205], 0
	v_mfma_i32_16x16x64_i8 v[90:93], v[94:97], v[210:213], 0
	v_mfma_i32_16x16x64_i8 v[66:69], v[102:105], v[210:213], 0
	v_mfma_i32_16x16x64_i8 v[154:157], v[98:101], v[180:183], v[154:157]
	v_mfma_i32_16x16x64_i8 v[146:149], v[106:109], v[180:183], v[146:149]
	v_mfma_i32_16x16x64_i8 v[138:141], v[98:101], v[198:201], v[138:141]
	v_mfma_i32_16x16x64_i8 v[130:133], v[106:109], v[198:201], v[130:133]
	v_mfma_i32_16x16x64_i8 v[122:125], v[98:101], v[206:209], v[122:125]
	v_mfma_i32_16x16x64_i8 v[114:117], v[106:109], v[206:209], v[114:117]
	v_mfma_i32_16x16x64_i8 v[90:93], v[98:101], v[214:217], v[90:93]
	v_mfma_i32_16x16x64_i8 v[66:69], v[106:109], v[214:217], v[66:69]
	s_setprio 0
	s_barrier
	s_add_i32 s42, s67, s57
	v_lshl_add_u64 v[184:185], s[46:47], 0, v[164:165]
	s_mov_b32 m0, s42
	ds_read_b128 v[176:179], v192 offset:16384
	ds_read_b128 v[180:183], v192 offset:17408
	ds_read_b128 v[194:197], v192 offset:18432
	ds_read_b128 v[198:201], v192 offset:19456
	ds_read_b128 v[202:205], v192 offset:20480
	ds_read_b128 v[206:209], v192 offset:21504
	ds_read_b128 v[210:213], v192 offset:22528
	ds_read_b128 v[214:217], v192 offset:23552
	global_load_lds_dwordx4 v[184:185], off
	s_add_i32 m0, s42, 0x2000
	s_add_u32 s42, s46, 0x40000
	v_lshl_add_u64 v[218:219], s[46:47], 0, v[166:167]
	s_addc_u32 s43, s47, 0
	s_add_i32 s72, s68, s57
	global_load_lds_dwordx4 v[218:219], off
	v_lshl_add_u64 v[220:221], s[42:43], 0, v[164:165]
	s_mov_b32 m0, s72
	v_mov_b32_e32 v169, v171
	global_load_lds_dwordx4 v[220:221], off
	v_lshl_add_u64 v[220:221], s[42:43], 0, v[166:167]
	s_add_i32 m0, s72, 0x2000
	v_lshl_add_u64 v[222:223], s[48:49], 0, v[168:169]
	global_load_lds_dwordx4 v[220:221], off
	s_mov_b32 m0, s11
	v_lshl_add_u64 v[220:221], s[48:49], 0, v[170:171]
	global_load_lds_dwordx4 v170, s[48:49]
	s_mov_b32 m0, s58
	s_nop 0
	global_load_lds_dwordx4 v168, s[48:49]
	s_waitcnt vmcnt(8)
	s_waitcnt lgkmcnt(0)
	s_barrier
	s_setprio 1
	s_waitcnt lgkmcnt(0)
	v_mfma_i32_16x16x64_i8 v[62:65], v[70:73], v[176:179], 0
	v_mfma_i32_16x16x64_i8 v[54:57], v[78:81], v[176:179], 0
	v_mfma_i32_16x16x64_i8 v[46:49], v[70:73], v[194:197], 0
	v_mfma_i32_16x16x64_i8 v[38:41], v[78:81], v[194:197], 0
	v_mfma_i32_16x16x64_i8 v[30:33], v[70:73], v[202:205], 0
	v_mfma_i32_16x16x64_i8 v[22:25], v[78:81], v[202:205], 0
	v_mfma_i32_16x16x64_i8 v[14:17], v[70:73], v[210:213], 0
	v_mfma_i32_16x16x64_i8 v[6:9], v[78:81], v[210:213], 0
	v_mfma_i32_16x16x64_i8 v[62:65], v[74:77], v[180:183], v[62:65]
	v_mfma_i32_16x16x64_i8 v[54:57], v[82:85], v[180:183], v[54:57]
	v_mfma_i32_16x16x64_i8 v[46:49], v[74:77], v[198:201], v[46:49]
	v_mfma_i32_16x16x64_i8 v[38:41], v[82:85], v[198:201], v[38:41]
	v_mfma_i32_16x16x64_i8 v[30:33], v[74:77], v[206:209], v[30:33]
	v_mfma_i32_16x16x64_i8 v[22:25], v[82:85], v[206:209], v[22:25]
	v_mfma_i32_16x16x64_i8 v[14:17], v[74:77], v[214:217], v[14:17]
	v_mfma_i32_16x16x64_i8 v[6:9], v[82:85], v[214:217], v[6:9]
	s_setprio 0
	s_setprio 1
	v_mfma_i32_16x16x64_i8 v[58:61], v[94:97], v[176:179], 0
	v_mfma_i32_16x16x64_i8 v[50:53], v[102:105], v[176:179], 0
	v_mfma_i32_16x16x64_i8 v[42:45], v[94:97], v[194:197], 0
	v_mfma_i32_16x16x64_i8 v[34:37], v[102:105], v[194:197], 0
	v_mfma_i32_16x16x64_i8 v[26:29], v[94:97], v[202:205], 0
	v_mfma_i32_16x16x64_i8 v[18:21], v[102:105], v[202:205], 0
	v_mfma_i32_16x16x64_i8 v[10:13], v[94:97], v[210:213], 0
	v_mfma_i32_16x16x64_i8 v[2:5], v[102:105], v[210:213], 0
	v_mfma_i32_16x16x64_i8 v[58:61], v[98:101], v[180:183], v[58:61]
	v_mfma_i32_16x16x64_i8 v[50:53], v[106:109], v[180:183], v[50:53]
	v_mfma_i32_16x16x64_i8 v[42:45], v[98:101], v[198:201], v[42:45]
	v_mfma_i32_16x16x64_i8 v[34:37], v[106:109], v[198:201], v[34:37]
	v_mfma_i32_16x16x64_i8 v[26:29], v[98:101], v[206:209], v[26:29]
	v_mfma_i32_16x16x64_i8 v[18:21], v[106:109], v[206:209], v[18:21]
	v_mfma_i32_16x16x64_i8 v[10:13], v[98:101], v[214:217], v[10:13]
	v_mfma_i32_16x16x64_i8 v[2:5], v[106:109], v[214:217], v[2:5]
	s_setprio 0
	s_barrier
	s_add_i32 s42, 0, 0x18000
	v_add_u32_e32 v0, s42, v189
	s_add_i32 s72, 0, 0x1c000
	ds_read_b128 v[70:73], v0
	ds_read_b128 v[74:77], v0 offset:1024
	ds_read_b128 v[78:81], v0 offset:2048
	ds_read_b128 v[82:85], v0 offset:3072
	v_add_u32_e32 v0, s72, v189
	ds_read_b128 v[94:97], v0
	ds_read_b128 v[98:101], v0 offset:1024
	ds_read_b128 v[102:105], v0 offset:2048
	ds_read_b128 v[106:109], v0 offset:3072
	s_mov_b32 m0, s59
	ds_read_b128 v[176:179], v192 offset:32768
	ds_read_b128 v[180:183], v192 offset:33792
	ds_read_b128 v[194:197], v192 offset:34816
	ds_read_b128 v[198:201], v192 offset:35840
	ds_read_b128 v[202:205], v192 offset:36864
	ds_read_b128 v[206:209], v192 offset:37888
	ds_read_b128 v[210:213], v192 offset:38912
	ds_read_b128 v[214:217], v192 offset:39936
	global_load_lds_dwordx4 v187, s[48:49]
	s_mov_b32 m0, s60
	s_nop 0
	global_load_lds_dwordx4 v186, s[48:49]
	s_waitcnt vmcnt(8)
	s_waitcnt lgkmcnt(0)
	s_barrier
	s_setprio 1
	s_waitcnt lgkmcnt(0)
	v_mfma_i32_16x16x64_i8 v[158:161], v[70:73], v[176:179], v[158:161]
	v_mfma_i32_16x16x64_i8 v[150:153], v[78:81], v[176:179], v[150:153]
	v_mfma_i32_16x16x64_i8 v[142:145], v[70:73], v[194:197], v[142:145]
	v_mfma_i32_16x16x64_i8 v[134:137], v[78:81], v[194:197], v[134:137]
	v_mfma_i32_16x16x64_i8 v[126:129], v[70:73], v[202:205], v[126:129]
	v_mfma_i32_16x16x64_i8 v[118:121], v[78:81], v[202:205], v[118:121]
	v_mfma_i32_16x16x64_i8 v[110:113], v[70:73], v[210:213], v[110:113]
	v_mfma_i32_16x16x64_i8 v[86:89], v[78:81], v[210:213], v[86:89]
	v_mfma_i32_16x16x64_i8 v[158:161], v[74:77], v[180:183], v[158:161]
	v_mfma_i32_16x16x64_i8 v[150:153], v[82:85], v[180:183], v[150:153]
	v_mfma_i32_16x16x64_i8 v[142:145], v[74:77], v[198:201], v[142:145]
	v_mfma_i32_16x16x64_i8 v[134:137], v[82:85], v[198:201], v[134:137]
	v_mfma_i32_16x16x64_i8 v[126:129], v[74:77], v[206:209], v[126:129]
	v_mfma_i32_16x16x64_i8 v[118:121], v[82:85], v[206:209], v[118:121]
	v_mfma_i32_16x16x64_i8 v[110:113], v[74:77], v[214:217], v[110:113]
	v_mfma_i32_16x16x64_i8 v[86:89], v[82:85], v[214:217], v[86:89]
	s_setprio 0
	s_setprio 1
	v_mfma_i32_16x16x64_i8 v[154:157], v[94:97], v[176:179], v[154:157]
	v_mfma_i32_16x16x64_i8 v[146:149], v[102:105], v[176:179], v[146:149]
	v_mfma_i32_16x16x64_i8 v[138:141], v[94:97], v[194:197], v[138:141]
	v_mfma_i32_16x16x64_i8 v[130:133], v[102:105], v[194:197], v[130:133]
	v_mfma_i32_16x16x64_i8 v[122:125], v[94:97], v[202:205], v[122:125]
	v_mfma_i32_16x16x64_i8 v[114:117], v[102:105], v[202:205], v[114:117]
	v_mfma_i32_16x16x64_i8 v[90:93], v[94:97], v[210:213], v[90:93]
	v_mfma_i32_16x16x64_i8 v[66:69], v[102:105], v[210:213], v[66:69]
	v_mfma_i32_16x16x64_i8 v[154:157], v[98:101], v[180:183], v[154:157]
	v_mfma_i32_16x16x64_i8 v[146:149], v[106:109], v[180:183], v[146:149]
	v_mfma_i32_16x16x64_i8 v[138:141], v[98:101], v[198:201], v[138:141]
	v_mfma_i32_16x16x64_i8 v[130:133], v[106:109], v[198:201], v[130:133]
	v_mfma_i32_16x16x64_i8 v[122:125], v[98:101], v[206:209], v[122:125]
	v_mfma_i32_16x16x64_i8 v[114:117], v[106:109], v[206:209], v[114:117]
	v_mfma_i32_16x16x64_i8 v[90:93], v[98:101], v[214:217], v[90:93]
	v_mfma_i32_16x16x64_i8 v[66:69], v[106:109], v[214:217], v[66:69]
	s_setprio 0
	s_barrier
	s_add_i32 s42, s42, s57
	v_lshl_add_u64 v[184:185], v[184:185], 0, s[22:23]
	s_mov_b32 m0, s42
	ds_read_b128 v[176:179], v192 offset:49152
	ds_read_b128 v[180:183], v192 offset:50176
	ds_read_b128 v[194:197], v192 offset:51200
	ds_read_b128 v[198:201], v192 offset:52224
	ds_read_b128 v[202:205], v192 offset:53248
	ds_read_b128 v[206:209], v192 offset:54272
	ds_read_b128 v[210:213], v192 offset:55296
	ds_read_b128 v[214:217], v192 offset:56320
	global_load_lds_dwordx4 v[184:185], off
	s_add_i32 m0, s42, 0x2000
	s_add_u32 s42, s46, 0x40080
	v_lshl_add_u64 v[184:185], v[218:219], 0, s[22:23]
	s_addc_u32 s43, s47, 0
	s_add_i32 s46, s72, s57
	global_load_lds_dwordx4 v[184:185], off
	v_lshl_add_u64 v[184:185], s[42:43], 0, v[164:165]
	s_mov_b32 m0, s46
	s_nop 0
	global_load_lds_dwordx4 v[184:185], off
	v_lshl_add_u64 v[184:185], s[42:43], 0, v[166:167]
	s_add_i32 m0, s46, 0x2000
	s_nop 0
	global_load_lds_dwordx4 v[184:185], off
	v_lshl_add_u64 v[184:185], v[220:221], 0, s[22:23]
	s_mov_b32 m0, s63
	s_nop 0
	global_load_lds_dwordx4 v[184:185], off
	v_lshl_add_u64 v[184:185], v[222:223], 0, s[22:23]
	s_mov_b32 m0, s64
	s_nop 0
	global_load_lds_dwordx4 v[184:185], off
	s_waitcnt vmcnt(8)
	s_waitcnt lgkmcnt(0)
	s_barrier
	s_setprio 1
	s_waitcnt lgkmcnt(0)
	v_mfma_i32_16x16x64_i8 v[62:65], v[70:73], v[176:179], v[62:65]
	v_mfma_i32_16x16x64_i8 v[54:57], v[78:81], v[176:179], v[54:57]
	v_mfma_i32_16x16x64_i8 v[46:49], v[70:73], v[194:197], v[46:49]
	v_mfma_i32_16x16x64_i8 v[38:41], v[78:81], v[194:197], v[38:41]
	v_mfma_i32_16x16x64_i8 v[30:33], v[70:73], v[202:205], v[30:33]
	v_mfma_i32_16x16x64_i8 v[22:25], v[78:81], v[202:205], v[22:25]
	v_mfma_i32_16x16x64_i8 v[14:17], v[70:73], v[210:213], v[14:17]
	v_mfma_i32_16x16x64_i8 v[6:9], v[78:81], v[210:213], v[6:9]
	v_mfma_i32_16x16x64_i8 v[62:65], v[74:77], v[180:183], v[62:65]
	v_mfma_i32_16x16x64_i8 v[54:57], v[82:85], v[180:183], v[54:57]
	v_mfma_i32_16x16x64_i8 v[46:49], v[74:77], v[198:201], v[46:49]
	v_mfma_i32_16x16x64_i8 v[38:41], v[82:85], v[198:201], v[38:41]
	v_mfma_i32_16x16x64_i8 v[30:33], v[74:77], v[206:209], v[30:33]
	v_mfma_i32_16x16x64_i8 v[22:25], v[82:85], v[206:209], v[22:25]
	v_mfma_i32_16x16x64_i8 v[14:17], v[74:77], v[214:217], v[14:17]
	v_mfma_i32_16x16x64_i8 v[6:9], v[82:85], v[214:217], v[6:9]
	s_setprio 0
	s_setprio 1
	v_mfma_i32_16x16x64_i8 v[58:61], v[94:97], v[176:179], v[58:61]
	v_mfma_i32_16x16x64_i8 v[50:53], v[102:105], v[176:179], v[50:53]
	v_mfma_i32_16x16x64_i8 v[42:45], v[94:97], v[194:197], v[42:45]
	v_mfma_i32_16x16x64_i8 v[34:37], v[102:105], v[194:197], v[34:37]
	v_mfma_i32_16x16x64_i8 v[26:29], v[94:97], v[202:205], v[26:29]
	v_mfma_i32_16x16x64_i8 v[18:21], v[102:105], v[202:205], v[18:21]
	v_mfma_i32_16x16x64_i8 v[10:13], v[94:97], v[210:213], v[10:13]
	v_mfma_i32_16x16x64_i8 v[2:5], v[102:105], v[210:213], v[2:5]
	v_mfma_i32_16x16x64_i8 v[58:61], v[98:101], v[180:183], v[58:61]
	v_mfma_i32_16x16x64_i8 v[50:53], v[106:109], v[180:183], v[50:53]
	v_mfma_i32_16x16x64_i8 v[42:45], v[98:101], v[198:201], v[42:45]
	v_mfma_i32_16x16x64_i8 v[34:37], v[106:109], v[198:201], v[34:37]
	v_mfma_i32_16x16x64_i8 v[26:29], v[98:101], v[206:209], v[26:29]
	v_mfma_i32_16x16x64_i8 v[18:21], v[106:109], v[206:209], v[18:21]
	v_mfma_i32_16x16x64_i8 v[10:13], v[98:101], v[214:217], v[10:13]
	v_mfma_i32_16x16x64_i8 v[2:5], v[106:109], v[214:217], v[2:5]
	s_setprio 0
	s_barrier
	s_add_i32 s39, s39, 2
	s_cmp_gt_u32 s39, 13
	s_mov_b64 s[42:43], s[44:45]
	s_cbranch_scc0 .LBB0_1214
	s_branch .Lkexit_1214
	s_nop 0
	s_nop 0
	s_nop 0
	s_nop 0
	s_nop 0
	s_nop 0
	s_nop 0
	s_nop 0
	s_nop 0
	s_nop 0
	s_nop 0
	s_nop 0
	s_nop 0
	s_nop 0
	s_nop 0
	s_nop 0
	s_nop 0
	s_nop 0
	s_nop 0
	s_nop 0
	s_nop 0
	s_nop 0
	s_nop 0
	s_nop 0
	s_nop 0
	s_nop 0
	s_nop 0

.LBB0_1366:
	s_lshl_b64 s[36:37], s[28:29], 19
	s_add_u32 s36, s2, s36
	s_addc_u32 s37, s3, s37
	s_and_b64 s[0:1], exec, s[0:1]
	s_cselect_b32 s27, s37, s43
	s_cselect_b32 s29, s36, s42
	s_add_u32 s0, s42, 0x40080
	s_addc_u32 s1, s43, 0
	s_add_u32 s31, s40, 0x100
	s_addc_u32 s39, s41, 0
	s_mov_b32 s61, -2
	ds_read_b128 v[66:69], v229
	ds_read_b128 v[70:73], v229 offset:1024
	ds_read_b128 v[82:85], v229 offset:2048
	ds_read_b128 v[86:89], v229 offset:3072
	ds_read_b128 v[90:93], v230
	ds_read_b128 v[94:97], v230 offset:1024
	ds_read_b128 v[98:101], v230 offset:2048
	ds_read_b128 v[102:105], v230 offset:3072
	s_add_u32 s40, s0, 0xfffc0080
	s_addc_u32 s41, s1, -1
	s_cmp_eq_u32 s61, 12
	s_cselect_b32 s43, s27, s41
	s_cselect_b32 s42, s29, s40
	s_cselect_b32 s41, s35, s39
	s_cselect_b32 s40, s34, s31
	v_lshl_add_u64 v[208:209], s[0:1], 0, v[170:171]
	s_add_i32 m0, s15, 0xc000
	ds_read_b128 v[176:179], v231
	ds_read_b128 v[180:183], v231 offset:1024
	ds_read_b128 v[184:187], v231 offset:2048
	ds_read_b128 v[188:191], v231 offset:3072
	ds_read_b128 v[192:195], v231 offset:4096
	ds_read_b128 v[196:199], v231 offset:5120
	ds_read_b128 v[200:203], v231 offset:6144
	ds_read_b128 v[204:207], v231 offset:7168
	global_load_lds_dwordx4 v[208:209], off
	v_lshl_add_u64 v[208:209], s[0:1], 0, v[172:173]
	s_add_i32 m0, s15, 0xe000
	s_nop 0
	global_load_lds_dwordx4 v[208:209], off
	s_waitcnt vmcnt(32)
	s_waitcnt lgkmcnt(0)
	s_barrier
	s_setprio 1
	s_waitcnt lgkmcnt(0)
	v_mfma_i32_16x16x64_i8 v[158:161], v[66:69], v[176:179], 0
	v_mfma_i32_16x16x64_i8 v[154:157], v[82:85], v[176:179], 0
	v_mfma_i32_16x16x64_i8 v[142:145], v[66:69], v[184:187], 0
	v_mfma_i32_16x16x64_i8 v[138:141], v[82:85], v[184:187], 0
	v_mfma_i32_16x16x64_i8 v[126:129], v[66:69], v[192:195], 0
	v_mfma_i32_16x16x64_i8 v[122:125], v[82:85], v[192:195], 0
	v_mfma_i32_16x16x64_i8 v[110:113], v[66:69], v[200:203], 0
	v_mfma_i32_16x16x64_i8 v[106:109], v[82:85], v[200:203], 0
	v_mfma_i32_16x16x64_i8 v[158:161], v[70:73], v[180:183], v[158:161]
	v_mfma_i32_16x16x64_i8 v[154:157], v[86:89], v[180:183], v[154:157]
	v_mfma_i32_16x16x64_i8 v[142:145], v[70:73], v[188:191], v[142:145]
	v_mfma_i32_16x16x64_i8 v[138:141], v[86:89], v[188:191], v[138:141]
	v_mfma_i32_16x16x64_i8 v[126:129], v[70:73], v[196:199], v[126:129]
	v_mfma_i32_16x16x64_i8 v[122:125], v[86:89], v[196:199], v[122:125]
	v_mfma_i32_16x16x64_i8 v[110:113], v[70:73], v[204:207], v[110:113]
	v_mfma_i32_16x16x64_i8 v[106:109], v[86:89], v[204:207], v[106:109]
	s_setprio 0
	s_setprio 1
	v_mfma_i32_16x16x64_i8 v[150:153], v[90:93], v[176:179], 0
	v_mfma_i32_16x16x64_i8 v[146:149], v[98:101], v[176:179], 0
	v_mfma_i32_16x16x64_i8 v[134:137], v[90:93], v[184:187], 0
	v_mfma_i32_16x16x64_i8 v[130:133], v[98:101], v[184:187], 0
	v_mfma_i32_16x16x64_i8 v[118:121], v[90:93], v[192:195], 0
	v_mfma_i32_16x16x64_i8 v[114:117], v[98:101], v[192:195], 0
	v_mfma_i32_16x16x64_i8 v[78:81], v[90:93], v[200:203], 0
	v_mfma_i32_16x16x64_i8 v[74:77], v[98:101], v[200:203], 0
	v_mfma_i32_16x16x64_i8 v[150:153], v[94:97], v[180:183], v[150:153]
	v_mfma_i32_16x16x64_i8 v[146:149], v[102:105], v[180:183], v[146:149]
	v_mfma_i32_16x16x64_i8 v[134:137], v[94:97], v[188:191], v[134:137]
	v_mfma_i32_16x16x64_i8 v[130:133], v[102:105], v[188:191], v[130:133]
	v_mfma_i32_16x16x64_i8 v[118:121], v[94:97], v[196:199], v[118:121]
	v_mfma_i32_16x16x64_i8 v[114:117], v[102:105], v[196:199], v[114:117]
	v_mfma_i32_16x16x64_i8 v[78:81], v[94:97], v[204:207], v[78:81]
	v_mfma_i32_16x16x64_i8 v[74:77], v[102:105], v[204:207], v[74:77]
	s_setprio 0
	s_barrier
	s_add_i32 s62, s57, s47
	v_lshl_add_u64 v[208:209], s[40:41], 0, v[164:165]
	s_mov_b32 m0, s62
	ds_read_b128 v[176:179], v231 offset:16384
	ds_read_b128 v[180:183], v231 offset:17408
	ds_read_b128 v[184:187], v231 offset:18432
	ds_read_b128 v[188:191], v231 offset:19456
	ds_read_b128 v[192:195], v231 offset:20480
	ds_read_b128 v[196:199], v231 offset:21504
	ds_read_b128 v[200:203], v231 offset:22528
	ds_read_b128 v[204:207], v231 offset:23552
	global_load_lds_dwordx4 v[208:209], off
	s_add_i32 m0, s62, 0x2000
	s_add_u32 s62, s40, 0x40000
	v_lshl_add_u64 v[210:211], s[40:41], 0, v[168:169]
	s_addc_u32 s63, s41, 0
	s_add_i32 s64, s58, s47
	global_load_lds_dwordx4 v[210:211], off
	v_lshl_add_u64 v[212:213], s[62:63], 0, v[164:165]
	s_mov_b32 m0, s64
	v_lshl_add_u64 v[214:215], s[42:43], 0, v[166:167]
	global_load_lds_dwordx4 v[212:213], off
	v_lshl_add_u64 v[212:213], s[62:63], 0, v[168:169]
	s_add_i32 m0, s64, 0x2000
	s_nop 0
	global_load_lds_dwordx4 v[212:213], off
	v_lshl_add_u64 v[212:213], s[42:43], 0, v[162:163]
	s_mov_b32 m0, s15
	s_nop 0
	global_load_lds_dwordx4 v[212:213], off
	s_mov_b32 m0, s48
	s_nop 0
	global_load_lds_dwordx4 v[214:215], off
	s_waitcnt vmcnt(8)
	s_waitcnt lgkmcnt(0)
	s_barrier
	s_setprio 1
	s_waitcnt lgkmcnt(0)
	v_mfma_i32_16x16x64_i8 v[62:65], v[66:69], v[176:179], 0
	v_mfma_i32_16x16x64_i8 v[58:61], v[82:85], v[176:179], 0
	v_mfma_i32_16x16x64_i8 v[46:49], v[66:69], v[184:187], 0
	v_mfma_i32_16x16x64_i8 v[42:45], v[82:85], v[184:187], 0
	v_mfma_i32_16x16x64_i8 v[30:33], v[66:69], v[192:195], 0
	v_mfma_i32_16x16x64_i8 v[26:29], v[82:85], v[192:195], 0
	v_mfma_i32_16x16x64_i8 v[14:17], v[66:69], v[200:203], 0
	v_mfma_i32_16x16x64_i8 v[10:13], v[82:85], v[200:203], 0
	v_mfma_i32_16x16x64_i8 v[62:65], v[70:73], v[180:183], v[62:65]
	v_mfma_i32_16x16x64_i8 v[58:61], v[86:89], v[180:183], v[58:61]
	v_mfma_i32_16x16x64_i8 v[46:49], v[70:73], v[188:191], v[46:49]
	v_mfma_i32_16x16x64_i8 v[42:45], v[86:89], v[188:191], v[42:45]
	v_mfma_i32_16x16x64_i8 v[30:33], v[70:73], v[196:199], v[30:33]
	v_mfma_i32_16x16x64_i8 v[26:29], v[86:89], v[196:199], v[26:29]
	v_mfma_i32_16x16x64_i8 v[14:17], v[70:73], v[204:207], v[14:17]
	v_mfma_i32_16x16x64_i8 v[10:13], v[86:89], v[204:207], v[10:13]
	s_setprio 0
	s_setprio 1
	v_mfma_i32_16x16x64_i8 v[54:57], v[90:93], v[176:179], 0
	v_mfma_i32_16x16x64_i8 v[50:53], v[98:101], v[176:179], 0
	v_mfma_i32_16x16x64_i8 v[38:41], v[90:93], v[184:187], 0
	v_mfma_i32_16x16x64_i8 v[34:37], v[98:101], v[184:187], 0
	v_mfma_i32_16x16x64_i8 v[22:25], v[90:93], v[192:195], 0
	v_mfma_i32_16x16x64_i8 v[18:21], v[98:101], v[192:195], 0
	v_mfma_i32_16x16x64_i8 v[6:9], v[90:93], v[200:203], 0
	v_mfma_i32_16x16x64_i8 v[2:5], v[98:101], v[200:203], 0
	v_mfma_i32_16x16x64_i8 v[54:57], v[94:97], v[180:183], v[54:57]
	v_mfma_i32_16x16x64_i8 v[50:53], v[102:105], v[180:183], v[50:53]
	v_mfma_i32_16x16x64_i8 v[38:41], v[94:97], v[188:191], v[38:41]
	v_mfma_i32_16x16x64_i8 v[34:37], v[102:105], v[188:191], v[34:37]
	v_mfma_i32_16x16x64_i8 v[22:25], v[94:97], v[196:199], v[22:25]
	v_mfma_i32_16x16x64_i8 v[18:21], v[102:105], v[196:199], v[18:21]
	v_mfma_i32_16x16x64_i8 v[6:9], v[94:97], v[204:207], v[6:9]
	v_mfma_i32_16x16x64_i8 v[2:5], v[102:105], v[204:207], v[2:5]
	s_setprio 0
	s_barrier
	s_add_i32 s62, 0, 0x18000
	v_add_u32_e32 v0, s62, v227
	s_add_i32 s63, 0, 0x1c000
	ds_read_b128 v[66:69], v0
	ds_read_b128 v[70:73], v0 offset:1024
	ds_read_b128 v[82:85], v0 offset:2048
	ds_read_b128 v[86:89], v0 offset:3072
	v_add_u32_e32 v0, s63, v227
	ds_read_b128 v[90:93], v0
	ds_read_b128 v[94:97], v0 offset:1024
	ds_read_b128 v[98:101], v0 offset:2048
	ds_read_b128 v[102:105], v0 offset:3072
	s_add_u32 s42, s42, 0x40000
	s_addc_u32 s43, s43, 0
	s_mov_b32 m0, s49
	v_lshl_add_u64 v[216:217], s[42:43], 0, v[162:163]
	ds_read_b128 v[176:179], v231 offset:32768
	ds_read_b128 v[180:183], v231 offset:33792
	ds_read_b128 v[184:187], v231 offset:34816
	ds_read_b128 v[188:191], v231 offset:35840
	ds_read_b128 v[192:195], v231 offset:36864
	ds_read_b128 v[196:199], v231 offset:37888
	ds_read_b128 v[200:203], v231 offset:38912
	ds_read_b128 v[204:207], v231 offset:39936
	global_load_lds_dwordx4 v[216:217], off
	v_lshl_add_u64 v[216:217], s[42:43], 0, v[166:167]
	s_mov_b32 m0, s51
	s_nop 0
	global_load_lds_dwordx4 v[216:217], off
	s_waitcnt vmcnt(8)
	s_waitcnt lgkmcnt(0)
	s_barrier
	s_setprio 1
	s_waitcnt lgkmcnt(0)
	v_mfma_i32_16x16x64_i8 v[158:161], v[66:69], v[176:179], v[158:161]
	v_mfma_i32_16x16x64_i8 v[154:157], v[82:85], v[176:179], v[154:157]
	v_mfma_i32_16x16x64_i8 v[142:145], v[66:69], v[184:187], v[142:145]
	v_mfma_i32_16x16x64_i8 v[138:141], v[82:85], v[184:187], v[138:141]
	v_mfma_i32_16x16x64_i8 v[126:129], v[66:69], v[192:195], v[126:129]
	v_mfma_i32_16x16x64_i8 v[122:125], v[82:85], v[192:195], v[122:125]
	v_mfma_i32_16x16x64_i8 v[110:113], v[66:69], v[200:203], v[110:113]
	v_mfma_i32_16x16x64_i8 v[106:109], v[82:85], v[200:203], v[106:109]
	v_mfma_i32_16x16x64_i8 v[158:161], v[70:73], v[180:183], v[158:161]
	v_mfma_i32_16x16x64_i8 v[154:157], v[86:89], v[180:183], v[154:157]
	v_mfma_i32_16x16x64_i8 v[142:145], v[70:73], v[188:191], v[142:145]
	v_mfma_i32_16x16x64_i8 v[138:141], v[86:89], v[188:191], v[138:141]
	v_mfma_i32_16x16x64_i8 v[126:129], v[70:73], v[196:199], v[126:129]
	v_mfma_i32_16x16x64_i8 v[122:125], v[86:89], v[196:199], v[122:125]
	v_mfma_i32_16x16x64_i8 v[110:113], v[70:73], v[204:207], v[110:113]
	v_mfma_i32_16x16x64_i8 v[106:109], v[86:89], v[204:207], v[106:109]
	s_setprio 0
	s_setprio 1
	v_mfma_i32_16x16x64_i8 v[150:153], v[90:93], v[176:179], v[150:153]
	v_mfma_i32_16x16x64_i8 v[146:149], v[98:101], v[176:179], v[146:149]
	v_mfma_i32_16x16x64_i8 v[134:137], v[90:93], v[184:187], v[134:137]
	v_mfma_i32_16x16x64_i8 v[130:133], v[98:101], v[184:187], v[130:133]
	v_mfma_i32_16x16x64_i8 v[118:121], v[90:93], v[192:195], v[118:121]
	v_mfma_i32_16x16x64_i8 v[114:117], v[98:101], v[192:195], v[114:117]
	v_mfma_i32_16x16x64_i8 v[78:81], v[90:93], v[200:203], v[78:81]
	v_mfma_i32_16x16x64_i8 v[74:77], v[98:101], v[200:203], v[74:77]
	v_mfma_i32_16x16x64_i8 v[150:153], v[94:97], v[180:183], v[150:153]
	v_mfma_i32_16x16x64_i8 v[146:149], v[102:105], v[180:183], v[146:149]
	v_mfma_i32_16x16x64_i8 v[134:137], v[94:97], v[188:191], v[134:137]
	v_mfma_i32_16x16x64_i8 v[130:133], v[102:105], v[188:191], v[130:133]
	v_mfma_i32_16x16x64_i8 v[118:121], v[94:97], v[196:199], v[118:121]
	v_mfma_i32_16x16x64_i8 v[114:117], v[102:105], v[196:199], v[114:117]
	v_mfma_i32_16x16x64_i8 v[78:81], v[94:97], v[204:207], v[78:81]
	v_mfma_i32_16x16x64_i8 v[74:77], v[102:105], v[204:207], v[74:77]
	s_setprio 0
	s_barrier
	s_add_i32 s42, s62, s47
	v_lshl_add_u64 v[208:209], v[208:209], 0, s[22:23]
	s_mov_b32 m0, s42
	ds_read_b128 v[176:179], v231 offset:49152
	ds_read_b128 v[180:183], v231 offset:50176
	ds_read_b128 v[184:187], v231 offset:51200
	ds_read_b128 v[188:191], v231 offset:52224
	ds_read_b128 v[192:195], v231 offset:53248
	ds_read_b128 v[196:199], v231 offset:54272
	ds_read_b128 v[200:203], v231 offset:55296
	ds_read_b128 v[204:207], v231 offset:56320
	global_load_lds_dwordx4 v[208:209], off
	s_add_i32 m0, s42, 0x2000
	s_add_u32 s40, s40, 0x40080
	v_lshl_add_u64 v[208:209], v[210:211], 0, s[22:23]
	s_addc_u32 s41, s41, 0
	s_add_i32 s42, s63, s47
	global_load_lds_dwordx4 v[208:209], off
	v_lshl_add_u64 v[208:209], s[40:41], 0, v[164:165]
	s_mov_b32 m0, s42
	s_nop 0
	global_load_lds_dwordx4 v[208:209], off
	v_lshl_add_u64 v[208:209], s[40:41], 0, v[168:169]
	s_add_i32 m0, s42, 0x2000
	s_nop 0
	global_load_lds_dwordx4 v[208:209], off
	v_lshl_add_u64 v[208:209], v[212:213], 0, s[22:23]
	s_mov_b32 m0, s53
	s_nop 0
	global_load_lds_dwordx4 v[208:209], off
	v_lshl_add_u64 v[208:209], v[214:215], 0, s[22:23]
	s_mov_b32 m0, s54
	s_nop 0
	global_load_lds_dwordx4 v[208:209], off
	s_waitcnt vmcnt(8)
	s_waitcnt lgkmcnt(0)
	s_barrier
	s_setprio 1
	s_waitcnt lgkmcnt(0)
	v_mfma_i32_16x16x64_i8 v[62:65], v[66:69], v[176:179], v[62:65]
	v_mfma_i32_16x16x64_i8 v[58:61], v[82:85], v[176:179], v[58:61]
	v_mfma_i32_16x16x64_i8 v[46:49], v[66:69], v[184:187], v[46:49]
	v_mfma_i32_16x16x64_i8 v[42:45], v[82:85], v[184:187], v[42:45]
	v_mfma_i32_16x16x64_i8 v[30:33], v[66:69], v[192:195], v[30:33]
	v_mfma_i32_16x16x64_i8 v[26:29], v[82:85], v[192:195], v[26:29]
	v_mfma_i32_16x16x64_i8 v[14:17], v[66:69], v[200:203], v[14:17]
	v_mfma_i32_16x16x64_i8 v[10:13], v[82:85], v[200:203], v[10:13]
	v_mfma_i32_16x16x64_i8 v[62:65], v[70:73], v[180:183], v[62:65]
	v_mfma_i32_16x16x64_i8 v[58:61], v[86:89], v[180:183], v[58:61]
	v_mfma_i32_16x16x64_i8 v[46:49], v[70:73], v[188:191], v[46:49]
	v_mfma_i32_16x16x64_i8 v[42:45], v[86:89], v[188:191], v[42:45]
	v_mfma_i32_16x16x64_i8 v[30:33], v[70:73], v[196:199], v[30:33]
	v_mfma_i32_16x16x64_i8 v[26:29], v[86:89], v[196:199], v[26:29]
	v_mfma_i32_16x16x64_i8 v[14:17], v[70:73], v[204:207], v[14:17]
	v_mfma_i32_16x16x64_i8 v[10:13], v[86:89], v[204:207], v[10:13]
	s_setprio 0
	s_setprio 1
	v_mfma_i32_16x16x64_i8 v[54:57], v[90:93], v[176:179], v[54:57]
	v_mfma_i32_16x16x64_i8 v[50:53], v[98:101], v[176:179], v[50:53]
	v_mfma_i32_16x16x64_i8 v[38:41], v[90:93], v[184:187], v[38:41]
	v_mfma_i32_16x16x64_i8 v[34:37], v[98:101], v[184:187], v[34:37]
	v_mfma_i32_16x16x64_i8 v[22:25], v[90:93], v[192:195], v[22:25]
	v_mfma_i32_16x16x64_i8 v[18:21], v[98:101], v[192:195], v[18:21]
	v_mfma_i32_16x16x64_i8 v[6:9], v[90:93], v[200:203], v[6:9]
	v_mfma_i32_16x16x64_i8 v[2:5], v[98:101], v[200:203], v[2:5]
	v_mfma_i32_16x16x64_i8 v[54:57], v[94:97], v[180:183], v[54:57]
	v_mfma_i32_16x16x64_i8 v[50:53], v[102:105], v[180:183], v[50:53]
	v_mfma_i32_16x16x64_i8 v[38:41], v[94:97], v[188:191], v[38:41]
	v_mfma_i32_16x16x64_i8 v[34:37], v[102:105], v[188:191], v[34:37]
	v_mfma_i32_16x16x64_i8 v[22:25], v[94:97], v[196:199], v[22:25]
	v_mfma_i32_16x16x64_i8 v[18:21], v[102:105], v[196:199], v[18:21]
	v_mfma_i32_16x16x64_i8 v[6:9], v[94:97], v[204:207], v[6:9]
	v_mfma_i32_16x16x64_i8 v[2:5], v[102:105], v[204:207], v[2:5]
	s_setprio 0
	s_barrier
	s_add_i32 s61, s61, 2
	s_add_u32 s0, s0, 0x100
	s_addc_u32 s1, s1, 0
	s_add_u32 s31, s31, 0x100
	s_addc_u32 s39, s39, 0
	s_cmp_gt_u32 s61, 13
	s_cbranch_scc0 .LBB0_1367
	s_branch .Lkexit_1367
	s_nop 0
	s_nop 0
	s_nop 0
	s_nop 0
	s_nop 0
	s_nop 0
	s_nop 0
	s_nop 0
	s_nop 0
	s_nop 0
	s_nop 0
	s_nop 0
	s_nop 0
	s_nop 0
	s_nop 0
	s_nop 0
	s_nop 0
	s_nop 0
	s_nop 0
	s_nop 0
	s_nop 0
	s_nop 0
	s_nop 0
